# baseline (speedup 1.0000x reference)
_Z16sum_layer_kernelPKfS0_Pf:
	s_load_dwordx4 s[4:7], s[0:1], 0x0
	s_load_dwordx2 s[8:9], s[0:1], 0x10
	v_bfe_u32 v41, v0, 5, 1
	v_and_b32_e32 v40, 31, v0
	s_lshl_b32 s0, s2, 10
	v_lshlrev_b32_e32 v1, 9, v41
	v_or3_b32 v1, v1, s0, v40
	s_waitcnt lgkmcnt(0)
	s_and_b32 s13, s7, 0xffff
	s_mov_b32 s15, 0x20000
	s_mov_b32 s14, 0x200000
	s_mov_b32 s12, s6
	v_lshlrev_b32_e32 v1, 2, v1
	buffer_load_dword v18, v1, s[12:15], 0 offen sc0 sc1 nt
	buffer_load_dword v19, v1, s[12:15], 0 offen offset:128 sc0 sc1 nt
	buffer_load_dword v20, v1, s[12:15], 0 offen offset:256 sc0 sc1 nt
	buffer_load_dword v21, v1, s[12:15], 0 offen offset:384 sc0 sc1 nt
	buffer_load_dword v22, v1, s[12:15], 0 offen offset:512 sc0 sc1 nt
	buffer_load_dword v23, v1, s[12:15], 0 offen offset:640 sc0 sc1 nt
	buffer_load_dword v24, v1, s[12:15], 0 offen offset:768 sc0 sc1 nt
	buffer_load_dword v25, v1, s[12:15], 0 offen offset:896 sc0 sc1 nt
	buffer_load_dword v26, v1, s[12:15], 0 offen offset:1024 sc0 sc1 nt
	buffer_load_dword v27, v1, s[12:15], 0 offen offset:1152 sc0 sc1 nt
	buffer_load_dword v28, v1, s[12:15], 0 offen offset:1280 sc0 sc1 nt
	buffer_load_dword v29, v1, s[12:15], 0 offen offset:1408 sc0 sc1 nt
	buffer_load_dword v30, v1, s[12:15], 0 offen offset:1536 sc0 sc1 nt
	buffer_load_dword v31, v1, s[12:15], 0 offen offset:1664 sc0 sc1 nt
	buffer_load_dword v32, v1, s[12:15], 0 offen offset:1792 sc0 sc1 nt
	s_nop 0
	buffer_load_dword v1, v1, s[12:15], 0 offen offset:1920 sc0 sc1 nt
	v_lshrrev_b32_e32 v42, 6, v0
	s_lshl_b32 s0, s2, 5
	v_lshlrev_b32_e32 v3, 2, v0
	v_lshl_add_u32 v2, v42, 19, s0
	v_and_b32_e32 v34, 28, v3
	v_or_b32_e32 v2, v2, v34
	v_bfe_u32 v33, v0, 3, 3
	v_lshlrev_b32_e32 v2, 2, v2
	s_and_b32 s5, s5, 0xffff
	s_mov_b32 s6, 0x800000
	s_mov_b32 s7, s15
	v_lshl_add_u32 v35, v33, 16, v2
	s_mov_b32 s0, 0x80000
	buffer_load_dwordx4 v[2:5], v35, s[4:7], 0 offen sc0 sc1 nt
	buffer_load_dwordx4 v[6:9], v35, s[4:7], s0 offen sc0 sc1 nt
	s_mov_b32 s0, 0x100000
	s_mov_b32 s1, 0x180000
	buffer_load_dwordx4 v[10:13], v35, s[4:7], s0 offen sc0 sc1 nt
	buffer_load_dwordx4 v[14:17], v35, s[4:7], s1 offen sc0 sc1 nt
	v_and_b32_e32 v35, 63, v0
	s_waitcnt vmcnt(18)
	v_max_f32_e32 v0, v19, v19
	v_max_f32_e32 v36, v18, v18
	v_max_f32_e32 v0, v36, v0
	s_waitcnt vmcnt(16)
	v_max3_f32 v0, v0, v20, v21
	s_waitcnt vmcnt(14)
	v_max3_f32 v0, v0, v22, v23
	s_waitcnt vmcnt(12)
	v_max3_f32 v0, v0, v24, v25
	s_waitcnt vmcnt(10)
	v_max3_f32 v0, v0, v26, v27
	s_waitcnt vmcnt(8)
	v_max3_f32 v0, v0, v28, v29
	s_waitcnt vmcnt(6)
	v_max3_f32 v0, v0, v30, v31
	s_waitcnt vmcnt(4)
	v_max3_f32 v0, v0, v32, v1
	v_mov_b32_e32 v36, v0
	s_nop 1
	v_permlane32_swap_b32_e32 v0, v36
	v_max_f32_e32 v36, v36, v36
	v_max_f32_e32 v0, v0, v0
	v_max_f32_e32 v0, v0, v36
	v_mov_b32_e32 v36, 0xc1600000
	s_mov_b32 s0, 0x3fb8aa3b
	v_fmamk_f32 v0, v0, 0x3fb8aa3b, v36
	v_fma_f32 v18, v18, s0, -v0
	v_exp_f32_e32 v37, v18
	v_fma_f32 v18, v19, s0, -v0
	v_exp_f32_e32 v38, v18
	v_fma_f32 v18, v20, s0, -v0
	v_exp_f32_e32 v20, v18
	v_fma_f32 v18, v21, s0, -v0
	v_exp_f32_e32 v21, v18
	v_fma_f32 v19, v22, s0, -v0
	v_add_f32_e32 v18, 0, v37
	v_exp_f32_e32 v22, v19
	v_fma_f32 v19, v23, s0, -v0
	v_add_f32_e32 v18, v18, v38
	v_exp_f32_e32 v39, v19
	v_fma_f32 v19, v24, s0, -v0
	v_add_f32_e32 v18, v18, v20
	v_exp_f32_e32 v23, v19
	v_fma_f32 v19, v25, s0, -v0
	v_add_f32_e32 v18, v18, v21
	v_exp_f32_e32 v24, v19
	v_fma_f32 v19, v26, s0, -v0
	v_add_f32_e32 v18, v18, v22
	v_exp_f32_e32 v43, v19
	v_fma_f32 v19, v27, s0, -v0
	v_add_f32_e32 v18, v18, v39
	v_exp_f32_e32 v44, v19
	v_fma_f32 v19, v28, s0, -v0
	v_add_f32_e32 v18, v18, v23
	v_exp_f32_e32 v45, v19
	v_fma_f32 v19, v29, s0, -v0
	v_add_f32_e32 v18, v18, v24
	v_exp_f32_e32 v46, v19
	v_fma_f32 v19, v30, s0, -v0
	v_add_f32_e32 v18, v18, v43
	v_exp_f32_e32 v47, v19
	v_fma_f32 v19, v31, s0, -v0
	v_add_f32_e32 v18, v18, v44
	v_exp_f32_e32 v48, v19
	v_fma_f32 v19, v32, s0, -v0
	v_add_f32_e32 v18, v18, v45
	v_exp_f32_e32 v49, v19
	v_fma_f32 v0, v1, s0, -v0
	v_add_f32_e32 v18, v18, v46
	v_exp_f32_e32 v50, v0
	v_add_f32_e32 v0, v18, v47
	v_add_f32_e32 v0, v0, v48
	v_add_f32_e32 v0, v0, v49
	v_add_f32_e32 v0, v0, v50
	v_mov_b32_e32 v1, v0
	s_nop 1
	v_permlane32_swap_b32_e32 v0, v1
	v_add_f32_e32 v0, v0, v1
	v_log_f32_e32 v0, v0
	s_nop 0
	v_add_f32_e32 v0, 0x41600000, v0
	v_mul_f32_e32 v25, 0xbf317218, v0
	v_mul_u32_u24_e32 v0, 0x1200, v42
	v_mul_u32_u24_e32 v1, 0x90, v33
	v_lshlrev_b32_e32 v18, 2, v34
	v_add3_u32 v1, v0, v1, v18
	s_waitcnt vmcnt(3)
	ds_write_b128 v1, v[2:5]
	s_waitcnt vmcnt(2)
	ds_write_b128 v1, v[6:9] offset:1152
	s_waitcnt vmcnt(1)
	ds_write_b128 v1, v[10:13] offset:2304
	s_waitcnt vmcnt(0)
	ds_write_b128 v1, v[14:17] offset:3456
	v_mul_u32_u24_e32 v1, 0x90, v40
	v_lshlrev_b32_e32 v2, 6, v41
	v_add3_u32 v12, v0, v1, v2
	ds_read_b128 v[0:3], v12
	ds_read_b128 v[4:7], v12 offset:16
	ds_read_b128 v[8:11], v12 offset:32
	ds_read_b128 v[16:19], v12 offset:48
	v_cmp_gt_u32_e32 vcc, 32, v35
	s_waitcnt lgkmcnt(3)
	v_max_f32_e32 v12, v1, v1
	v_max_f32_e32 v13, v0, v0
	v_max_f32_e32 v12, v13, v12
	v_max3_f32 v12, v12, v2, v3
	s_waitcnt lgkmcnt(2)
	v_max3_f32 v12, v12, v4, v5
	v_max3_f32 v12, v12, v6, v7
	s_waitcnt lgkmcnt(1)
	v_max3_f32 v12, v12, v8, v9
	v_max3_f32 v12, v12, v10, v11
	s_waitcnt lgkmcnt(0)
	v_max3_f32 v12, v12, v16, v17
	v_max3_f32 v12, v12, v18, v19
	v_mov_b32_e32 v13, v12
	s_nop 1
	v_permlane32_swap_b32_e32 v12, v13
	v_max_f32_e32 v13, v13, v13
	v_max_f32_e32 v12, v12, v12
	v_max_f32_e32 v12, v12, v13
	v_fmac_f32_e32 v36, 0x3fb8aa3b, v12
	v_fma_f32 v0, v0, s0, -v36
	v_cndmask_b32_e64 v13, v25, 1.0, vcc
	v_exp_f32_e32 v25, v0
	v_fma_f32 v0, v1, s0, -v36
	v_exp_f32_e32 v26, v0
	v_fma_f32 v0, v2, s0, -v36
	v_exp_f32_e32 v27, v0
	v_fma_f32 v0, v3, s0, -v36
	v_exp_f32_e32 v28, v0
	v_fma_f32 v0, v4, s0, -v36
	v_exp_f32_e32 v29, v0
	v_fma_f32 v0, v5, s0, -v36
	v_exp_f32_e32 v30, v0
	v_fma_f32 v0, v6, s0, -v36
	v_exp_f32_e32 v31, v0
	v_fma_f32 v0, v7, s0, -v36
	v_exp_f32_e32 v32, v0
	v_fma_f32 v16, v16, s0, -v36
	v_fma_f32 v0, v8, s0, -v36
	v_exp_f32_e32 v34, v16
	v_fma_f32 v16, v17, s0, -v36
	v_exp_f32_e32 v51, v0
	v_fma_f32 v0, v9, s0, -v36
	v_exp_f32_e32 v54, v16
	v_fma_f32 v16, v18, s0, -v36
	v_exp_f32_e32 v52, v0
	v_fma_f32 v0, v10, s0, -v36
	v_exp_f32_e32 v35, v16
	v_fma_f32 v16, v19, s0, -v36
	v_exp_f32_e32 v33, v0
	v_fma_f32 v0, v11, s0, -v36
	v_exp_f32_e32 v36, v16
	v_cvt_pk_f16_f32 v19, v31, v32
	v_cvt_pk_f16_f32 v18, v29, v30
	v_cvt_pk_f16_f32 v17, v27, v28
	v_cvt_pk_f16_f32 v16, v25, v26
	v_cndmask_b32_e32 v1, 1.0, v12, vcc
	v_exp_f32_e32 v53, v0
	v_cvt_pk_f16_f32 v23, v23, v24
	v_cvt_pk_f16_f32 v22, v22, v39
	v_cvt_pk_f16_f32 v21, v20, v21
	v_cvt_pk_f16_f32 v20, v37, v38
	v_cvt_pk_f16_f32 v35, v35, v36
	v_cvt_pk_f16_f32 v34, v34, v54
	v_mfma_f32_32x32x16_f16 v[16:31], v[16:19], v[20:23], 0
	v_cvt_pk_f16_f32 v33, v33, v53
	v_cvt_pk_f16_f32 v32, v51, v52
	v_cvt_pk_f16_f32 v39, v49, v50
	v_cvt_pk_f16_f32 v38, v47, v48
	v_cvt_pk_f16_f32 v37, v45, v46
	v_cvt_pk_f16_f32 v36, v43, v44
	s_lshl_b32 s0, s2, 7
	v_mfma_f32_32x32x2_f32 v[0:15], v1, v13, 0
	v_mfma_f32_32x32x16_f16 v[16:31], v[32:35], v[36:39], v[16:31]
	v_lshl_add_u32 v32, v42, 21, s0
	v_lshl_add_u32 v32, v41, 18, v32
	v_lshl_or_b32 v32, v40, 2, v32
	s_nop 8
	v_log_f32_e32 v16, v16
	v_log_f32_e32 v17, v17
	s_nop 2
	v_fmamk_f32 v0, v16, 0x3f317218, v0
	global_store_dword v32, v0, s[8:9]
	v_fmamk_f32 v0, v17, 0x3f317218, v1
	v_log_f32_e32 v1, v18
	v_add_u32_e32 v16, 0x10000, v32
	global_store_dword v16, v0, s[8:9]
	v_log_f32_e32 v0, v19
	v_fmamk_f32 v1, v1, 0x3f317218, v2
	v_add_u32_e32 v2, 0x20000, v32
	global_store_dword v2, v1, s[8:9]
	v_fmamk_f32 v0, v0, 0x3f317218, v3
	v_log_f32_e32 v1, v20
	v_add_u32_e32 v2, 0x30000, v32
	global_store_dword v2, v0, s[8:9]
	v_log_f32_e32 v0, v21
	v_fmamk_f32 v1, v1, 0x3f317218, v4
	v_add_u32_e32 v2, 0x80000, v32
	global_store_dword v2, v1, s[8:9]
	v_fmamk_f32 v0, v0, 0x3f317218, v5
	v_log_f32_e32 v1, v22
	v_add_u32_e32 v2, 0x90000, v32
	global_store_dword v2, v0, s[8:9]
	v_log_f32_e32 v0, v23
	v_fmamk_f32 v1, v1, 0x3f317218, v6
	v_add_u32_e32 v2, 0xa0000, v32
	global_store_dword v2, v1, s[8:9]
	v_fmamk_f32 v0, v0, 0x3f317218, v7
	v_log_f32_e32 v1, v24
	v_add_u32_e32 v2, 0xb0000, v32
	global_store_dword v2, v0, s[8:9]
	v_log_f32_e32 v0, v25
	v_fmamk_f32 v1, v1, 0x3f317218, v8
	v_add_u32_e32 v2, 0x100000, v32
	global_store_dword v2, v1, s[8:9]
	v_fmamk_f32 v0, v0, 0x3f317218, v9
	v_log_f32_e32 v1, v26
	v_add_u32_e32 v2, 0x110000, v32
	global_store_dword v2, v0, s[8:9]
	v_log_f32_e32 v0, v27
	v_fmamk_f32 v1, v1, 0x3f317218, v10
	v_add_u32_e32 v2, 0x120000, v32
	global_store_dword v2, v1, s[8:9]
	v_fmamk_f32 v0, v0, 0x3f317218, v11
	v_log_f32_e32 v1, v28
	v_add_u32_e32 v2, 0x130000, v32
	global_store_dword v2, v0, s[8:9]
	v_log_f32_e32 v0, v29
	v_fmamk_f32 v1, v1, 0x3f317218, v12
	v_add_u32_e32 v2, 0x180000, v32
	global_store_dword v2, v1, s[8:9]
	v_fmamk_f32 v0, v0, 0x3f317218, v13
	v_add_u32_e32 v2, 0x190000, v32
	v_log_f32_e32 v1, v30
	global_store_dword v2, v0, s[8:9]
	v_log_f32_e32 v0, v31
	v_add_u32_e32 v2, 0x1a0000, v32
	v_fmamk_f32 v1, v1, 0x3f317218, v14
	global_store_dword v2, v1, s[8:9]
	v_fmac_f32_e32 v15, 0x3f317218, v0
	v_add_u32_e32 v0, 0x1b0000, v32
	global_store_dword v0, v15, s[8:9]
	s_endpgm
